# speedup vs baseline: 1.0019x; 1.0019x over previous
_Z7k_gemm5PKDF16_S0_PKfPf:
	s_load_dwordx8 s[4:11], s[0:1], 0x0
	s_lshl_b32 s0, s2, 4
	s_ashr_i32 s16, s2, 6
	s_lshl_b32 s2, s2, 3
	v_lshrrev_b32_e32 v10, 4, v0
	s_and_b32 s34, s2, 0x1c0
	v_lshrrev_b32_e32 v1, 2, v0
	v_sub_u32_e32 v12, 0, v10
	v_xor_b32_e32 v4, v0, v12
	v_or_b32_e32 v1, s34, v1
	v_lshlrev_b32_e32 v66, 10, v1
	v_mov_b32_e32 v67, 0
	v_lshlrev_b32_e32 v1, 4, v4
	v_bfe_u32 v11, v0, 2, 2
	s_waitcnt lgkmcnt(0)
	v_lshl_add_u64 v[2:3], s[6:7], 0, v[66:67]
	v_and_b32_e32 v4, 48, v1
	v_mov_b32_e32 v5, v67
	v_lshl_add_u64 v[2:3], v[2:3], 0, v[4:5]
	v_sub_u32_e32 v4, 0, v11
	s_and_b32 s0, s0, 0x70
	v_and_b32_e32 v1, 30, v0
	v_xor_b32_e32 v4, v10, v4
	s_add_i32 s0, s0, s16
	v_bitop3_b32 v1, v10, v1, 14 bitop3:0x6c
	v_lshlrev_b32_e32 v4, 4, v4
	s_ashr_i32 s0, s0, 4
	s_lshl_b32 s1, s16, 8
	v_and_or_b32 v6, v0, 1, v1
	v_lshlrev_b32_e32 v1, 2, v10
	v_and_b32_e32 v15, 48, v4
	v_lshrrev_b32_e32 v4, 1, v0
	s_and_b32 s33, s1, 0xf00
	s_ashr_i32 s1, s0, 31
	v_and_b32_e32 v13, 4, v1
	v_and_b32_e32 v4, 16, v4
	s_lshl_b64 s[12:13], s[0:1], 22
	v_or3_b32 v8, v11, v4, v13
	v_lshlrev_b32_e32 v4, 3, v0
	s_add_u32 s14, s4, s12
	v_and_b32_e32 v9, 24, v4
	v_lshlrev_b32_e32 v4, 4, v0
	s_addc_u32 s15, s5, s13
	v_add_u32_e32 v135, 0, v4
	s_cmp_lg_u32 0, -1
	v_readfirstlane_b32 s2, v135
	v_add_u32_e32 v136, 0x1000, v135
	s_cselect_b32 s17, 0, 0
	s_mov_b32 m0, s2
	s_mov_b64 s[2:3], 0x80000
	v_readfirstlane_b32 s19, v136
	s_add_i32 s18, s17, 0x2000
	global_load_lds_dwordx4 v[2:3], off
	v_lshl_add_u64 v[2:3], v[2:3], 0, s[2:3]
	s_mov_b32 m0, s19
	s_lshl_b32 s19, s33, 1
	global_load_lds_dwordx4 v[2:3], off
	s_add_u32 s14, s14, s19
	v_lshlrev_b32_e32 v2, 8, v0
	s_addc_u32 s15, s15, 0
	v_and_b32_e32 v2, 0xe000, v2
	v_mov_b32_e32 v3, v67
	v_add_u32_e32 v137, 0x2000, v135
	v_lshl_add_u64 v[4:5], s[14:15], 0, v[2:3]
	v_lshlrev_b32_e32 v6, 4, v6
	v_mov_b32_e32 v7, v67
	v_readfirstlane_b32 s14, v137
	v_lshl_add_u64 v[4:5], v[4:5], 0, v[6:7]
	v_lshlrev_b32_e32 v3, 9, v8
	s_mov_b32 m0, s14
	s_mov_b64 s[14:15], 0x10000
	v_add_u32_e32 v138, 0x3000, v135
	v_add3_u32 v3, v9, s18, v3
	v_lshl_add_u64 v[8:9], v[4:5], 0, s[14:15]
	v_readfirstlane_b32 s14, v138
	global_load_lds_dwordx4 v[4:5], off
	s_mov_b32 m0, s14
	s_mov_b64 s[14:15], 0x20000
	v_add_u32_e32 v139, 0x4000, v135
	global_load_lds_dwordx4 v[8:9], off
	v_lshl_add_u64 v[8:9], v[4:5], 0, s[14:15]
	v_readfirstlane_b32 s14, v139
	s_mov_b32 m0, s14
	s_mov_b64 s[14:15], 0x30000
	v_add_u32_e32 v140, 0x5000, v135
	v_lshl_add_u64 v[4:5], v[4:5], 0, s[14:15]
	v_readfirstlane_b32 s14, v140
	global_load_lds_dwordx4 v[8:9], off
	s_mov_b32 m0, s14
	v_or_b32_e32 v2, s12, v2
	global_load_lds_dwordx4 v[4:5], off
	v_and_b32_e32 v4, 12, v10
	v_bitop3_b32 v4, v11, v13, v4 bitop3:0xf6
	v_lshlrev_b32_e32 v4, 5, v4
	v_xor_b32_e32 v7, 32, v4
	v_xor_b32_e32 v8, 64, v4
	v_xor_b32_e32 v9, 0x60, v4
	v_add_u32_e32 v5, 0x6000, v3
	v_add_u32_e32 v142, v4, v3
	v_add_u32_e32 v143, v7, v3
	v_add_u32_e32 v144, v8, v3
	v_add_u32_e32 v145, v9, v3
	v_bitop3_b32 v3, v0, 3, v12 bitop3:0x48
	v_lshl_or_b32 v66, v3, 4, v66
	v_add_u32_e32 v146, v5, v4
	v_add_u32_e32 v147, v5, v7
	v_add_u32_e32 v148, v5, v8
	v_add_u32_e32 v149, v5, v9
	v_lshl_add_u64 v[4:5], s[6:7], 0, v[66:67]
	s_mov_b64 s[6:7], 0x80080
	v_lshl_add_u64 v[130:131], v[4:5], 0, s[6:7]
	s_lshl_b32 s6, s16, 9
	s_and_b32 s6, s6, 0x1e00
	v_and_b32_e32 v134, 15, v0
	v_or3_b32 v2, v2, s6, v6
	v_mov_b32_e32 v3, s13
	v_lshlrev_b32_e32 v14, 6, v134
	v_lshl_add_u64 v[2:3], s[4:5], 0, v[2:3]
	s_mov_b64 s[4:5], 0xb0000
	v_add3_u32 v141, v14, s17, v15
	v_lshl_add_u64 v[132:133], v[2:3], 0, s[4:5]
	s_mov_b32 s4, 0xfff7ffc0
	s_movk_i32 s6, 0xffc0
	s_mov_b32 s12, 0xfff90000
	s_mov_b32 s14, 0xfffa0000
	s_mov_b32 s16, 0xfffb0000
	s_mov_b32 s18, 0xfffc0000
	s_mov_b32 s20, 0xfff80000
	s_mov_b32 s22, 0xfffd0000
	s_mov_b32 s24, 0xfffe0000
	s_mov_b32 s26, 0xffff0000
	s_mov_b32 s35, 0
	s_mov_b32 s5, -1
	s_mov_b32 s7, -1
	s_mov_b32 s13, -1
	s_mov_b32 s15, -1
	s_mov_b32 s17, -1
	s_mov_b32 s19, -1
	s_mov_b32 s21, -1
	s_mov_b32 s23, -1
	s_mov_b32 s25, -1
	s_mov_b32 s27, -1
	s_mov_b64 s[28:29], 0x80
	v_mov_b32_e32 v66, v67
	v_mov_b32_e32 v68, v67
	v_mov_b32_e32 v69, v67
	v_mov_b32_e32 v70, v67
	v_mov_b32_e32 v71, v67
	v_mov_b32_e32 v72, v67
	v_mov_b32_e32 v73, v67
	v_mov_b32_e32 v74, v67
	v_mov_b32_e32 v75, v67
	v_mov_b32_e32 v76, v67
	v_mov_b32_e32 v77, v67
	v_mov_b32_e32 v78, v67
	v_mov_b32_e32 v79, v67
	v_mov_b32_e32 v80, v67
	v_mov_b32_e32 v81, v67
	v_mov_b32_e32 v98, v67
	v_mov_b32_e32 v99, v67
	v_mov_b32_e32 v100, v67
	v_mov_b32_e32 v101, v67
	v_mov_b32_e32 v102, v67
	v_mov_b32_e32 v103, v67
	v_mov_b32_e32 v104, v67
	v_mov_b32_e32 v105, v67
	v_mov_b32_e32 v106, v67
	v_mov_b32_e32 v107, v67
	v_mov_b32_e32 v108, v67
	v_mov_b32_e32 v109, v67
	v_mov_b32_e32 v110, v67
	v_mov_b32_e32 v111, v67
	v_mov_b32_e32 v112, v67
	v_mov_b32_e32 v113, v67
	v_mov_b32_e32 v46, v67
	v_mov_b32_e32 v47, v67
	v_mov_b32_e32 v48, v67
	v_mov_b32_e32 v49, v67
	v_mov_b32_e32 v42, v67
	v_mov_b32_e32 v43, v67
	v_mov_b32_e32 v44, v67
	v_mov_b32_e32 v45, v67
	v_mov_b32_e32 v38, v67
	v_mov_b32_e32 v39, v67
	v_mov_b32_e32 v40, v67
	v_mov_b32_e32 v41, v67
	v_mov_b32_e32 v34, v67
	v_mov_b32_e32 v35, v67
	v_mov_b32_e32 v36, v67
	v_mov_b32_e32 v37, v67
	v_mov_b32_e32 v14, v67
	v_mov_b32_e32 v15, v67
	v_mov_b32_e32 v16, v67
	v_mov_b32_e32 v17, v67
	v_mov_b32_e32 v10, v67
	v_mov_b32_e32 v11, v67
	v_mov_b32_e32 v12, v67
	v_mov_b32_e32 v13, v67
	v_mov_b32_e32 v6, v67
	v_mov_b32_e32 v7, v67
	v_mov_b32_e32 v8, v67
	v_mov_b32_e32 v9, v67
	v_mov_b32_e32 v2, v67
	v_mov_b32_e32 v3, v67
	v_mov_b32_e32 v4, v67
	v_mov_b32_e32 v5, v67
	v_mov_b32_e32 v126, v67
	v_mov_b32_e32 v127, v67
	v_mov_b32_e32 v128, v67
	v_mov_b32_e32 v129, v67
	v_mov_b32_e32 v122, v67
	v_mov_b32_e32 v123, v67
	v_mov_b32_e32 v124, v67
	v_mov_b32_e32 v125, v67
	v_mov_b32_e32 v114, v67
	v_mov_b32_e32 v115, v67
	v_mov_b32_e32 v116, v67
	v_mov_b32_e32 v117, v67
	v_mov_b32_e32 v118, v67
	v_mov_b32_e32 v119, v67
	v_mov_b32_e32 v120, v67
	v_mov_b32_e32 v121, v67
	v_mov_b32_e32 v94, v67
	v_mov_b32_e32 v95, v67
	v_mov_b32_e32 v96, v67
	v_mov_b32_e32 v97, v67
	v_mov_b32_e32 v90, v67
	v_mov_b32_e32 v91, v67
	v_mov_b32_e32 v92, v67
	v_mov_b32_e32 v93, v67
	v_mov_b32_e32 v82, v67
	v_mov_b32_e32 v83, v67
	v_mov_b32_e32 v84, v67
	v_mov_b32_e32 v85, v67
	v_mov_b32_e32 v86, v67
	v_mov_b32_e32 v87, v67
	v_mov_b32_e32 v88, v67
	v_mov_b32_e32 v89, v67
	v_mov_b32_e32 v62, v67
	v_mov_b32_e32 v63, v67
	v_mov_b32_e32 v64, v67
	v_mov_b32_e32 v65, v67
	v_mov_b32_e32 v58, v67
	v_mov_b32_e32 v59, v67
	v_mov_b32_e32 v60, v67
	v_mov_b32_e32 v61, v67
	v_mov_b32_e32 v50, v67
	v_mov_b32_e32 v51, v67
	v_mov_b32_e32 v52, v67
	v_mov_b32_e32 v53, v67
	v_mov_b32_e32 v54, v67
	v_mov_b32_e32 v55, v67
	v_mov_b32_e32 v56, v67
	v_mov_b32_e32 v57, v67
	v_mov_b32_e32 v30, v67
	v_mov_b32_e32 v31, v67
	v_mov_b32_e32 v32, v67
	v_mov_b32_e32 v33, v67
	v_mov_b32_e32 v26, v67
	v_mov_b32_e32 v27, v67
	v_mov_b32_e32 v28, v67
	v_mov_b32_e32 v29, v67
	v_mov_b32_e32 v22, v67
	v_mov_b32_e32 v23, v67
	v_mov_b32_e32 v24, v67
	v_mov_b32_e32 v25, v67
	v_mov_b32_e32 v18, v67
	v_mov_b32_e32 v19, v67
	v_mov_b32_e32 v20, v67
	v_mov_b32_e32 v21, v67
	v_add_u32_e32 v150, 0x6000, v141
	v_add_u32_e32 v151, 0x6000, v135
	v_add_u32_e32 v152, 0x7000, v135
	v_add_u32_e32 v153, 0x8000, v135
	v_add_u32_e32 v154, 0x9000, v135
	v_add_u32_e32 v155, 0xa000, v135
	v_add_u32_e32 v156, 0xb000, v135
	s_nop 0
	s_nop 0
	s_nop 0
	s_nop 0
	s_waitcnt vmcnt(0) lgkmcnt(0)
	s_barrier
	s_branch .LBB8_2
